# speedup vs baseline: 1.0104x; 1.0064x over previous
.Llight_path:
	s_waitcnt vmcnt(16)
	v_mul_u32_u24_e32 v236, 36, v228
	v_add_u32_e32 v236, v236, v230
	v_add_u32_e32 v237, s7, v229
	v_mul_u32_u24_e32 v238, 0x104, v228
	v_add_u32_e32 v238, v238, v237
	v_add_u32_e32 v238, 0xb840, v238
	ds_read_b128 v[2:5], v237 offset:36928
	ds_read_b128 v[6:9], v237 offset:36944
	ds_read_b128 v[10:13], v237 offset:36960
	ds_read_b128 v[14:17], v237 offset:36976
	ds_read_b128 v[18:21], v237 offset:37056
	ds_read_b128 v[22:25], v237 offset:37072
	ds_read_b128 v[26:29], v237 offset:37088
	ds_read_b128 v[30:33], v237 offset:37104
	ds_read_b128 v[162:165], v236 offset:16384
	ds_read_b128 v[166:169], v236 offset:16416
	ds_read_b128 v[170:173], v236 offset:16448
	ds_read_b128 v[174:177], v236 offset:16480
	s_waitcnt lgkmcnt(0)
	v_mfma_f32_32x32x16_bf16 v[2:17], v[94:97], v[162:165], v[2:17]
	v_mfma_f32_32x32x16_bf16 v[2:17], v[90:93], v[166:169], v[2:17]
	v_mfma_f32_32x32x16_bf16 v[2:17], v[86:89], v[170:173], v[2:17]
	v_mfma_f32_32x32x16_bf16 v[2:17], v[82:85], v[174:177], v[2:17]
	v_mfma_f32_32x32x16_bf16 v[18:33], v[46:49], v[162:165], v[18:33]
	ds_read_b128 v[130:133], v237 offset:36928
	ds_read_b128 v[134:137], v237 offset:36944
	ds_read_b128 v[138:141], v237 offset:36960
	v_mfma_f32_32x32x16_bf16 v[18:33], v[42:45], v[166:169], v[18:33]
	ds_read_b128 v[142:145], v237 offset:36976
	ds_read_b128 v[146:149], v237 offset:37056
	ds_read_b128 v[150:153], v237 offset:37072
	v_mfma_f32_32x32x16_bf16 v[18:33], v[38:41], v[170:173], v[18:33]
	ds_read_b128 v[154:157], v237 offset:37088
	ds_read_b128 v[158:161], v237 offset:37104
	ds_read_b128 v[178:181], v236 offset:20992
	v_mfma_f32_32x32x16_bf16 v[18:33], v[34:37], v[174:177], v[18:33]
	ds_read_b128 v[182:185], v236 offset:21024
	ds_read_b128 v[186:189], v236 offset:21056
	ds_read_b128 v[190:193], v236 offset:21088
	s_waitcnt lgkmcnt(0)
	v_mfma_f32_32x32x16_bf16 v[130:145], v[94:97], v[178:181], v[130:145]
	v_mfma_f32_32x32x16_bf16 v[130:145], v[90:93], v[182:185], v[130:145]
	v_mfma_f32_32x32x16_bf16 v[130:145], v[86:89], v[186:189], v[130:145]
	v_mfma_f32_32x32x16_bf16 v[130:145], v[82:85], v[190:193], v[130:145]
	s_nop 7
	ds_write_b128 v238, v[2:5] offset:0
	ds_write_b128 v238, v[6:9] offset:16
	ds_write_b128 v238, v[10:13] offset:32
	ds_write_b128 v238, v[14:17] offset:48
	ds_write_b128 v238, v[18:21] offset:128
	ds_write_b128 v238, v[22:25] offset:144
	ds_write_b128 v238, v[26:29] offset:160
	ds_write_b128 v238, v[30:33] offset:176
	v_mfma_f32_32x32x16_bf16 v[146:161], v[46:49], v[178:181], v[146:161]
	ds_read_b128 v[2:5], v237 offset:36928
	ds_read_b128 v[6:9], v237 offset:36944
	ds_read_b128 v[10:13], v237 offset:36960
	v_mfma_f32_32x32x16_bf16 v[146:161], v[42:45], v[182:185], v[146:161]
	ds_read_b128 v[14:17], v237 offset:36976
	ds_read_b128 v[18:21], v237 offset:37056
	ds_read_b128 v[22:25], v237 offset:37072
	v_mfma_f32_32x32x16_bf16 v[146:161], v[38:41], v[186:189], v[146:161]
	ds_read_b128 v[26:29], v237 offset:37088
	ds_read_b128 v[30:33], v237 offset:37104
	ds_read_b128 v[162:165], v236 offset:25600
	v_mfma_f32_32x32x16_bf16 v[146:161], v[34:37], v[190:193], v[146:161]
	ds_read_b128 v[166:169], v236 offset:25632
	ds_read_b128 v[170:173], v236 offset:25664
	ds_read_b128 v[174:177], v236 offset:25696
	s_waitcnt lgkmcnt(0)
	v_mfma_f32_32x32x16_bf16 v[2:17], v[94:97], v[162:165], v[2:17]
	v_mfma_f32_32x32x16_bf16 v[2:17], v[90:93], v[166:169], v[2:17]
	v_mfma_f32_32x32x16_bf16 v[2:17], v[86:89], v[170:173], v[2:17]
	v_mfma_f32_32x32x16_bf16 v[2:17], v[82:85], v[174:177], v[2:17]
	s_nop 7
	v_add_u32_e32 v239, 0x8200, v238
	ds_write_b128 v239, v[130:133] offset:0
	ds_write_b128 v239, v[134:137] offset:16
	ds_write_b128 v239, v[138:141] offset:32
	ds_write_b128 v239, v[142:145] offset:48
	ds_write_b128 v239, v[146:149] offset:128
	ds_write_b128 v239, v[150:153] offset:144
	ds_write_b128 v239, v[154:157] offset:160
	ds_write_b128 v239, v[158:161] offset:176
	v_mfma_f32_32x32x16_bf16 v[18:33], v[46:49], v[162:165], v[18:33]
	ds_read_b128 v[130:133], v237 offset:36928
	ds_read_b128 v[134:137], v237 offset:36944
	ds_read_b128 v[138:141], v237 offset:36960
	v_mfma_f32_32x32x16_bf16 v[18:33], v[42:45], v[166:169], v[18:33]
	ds_read_b128 v[142:145], v237 offset:36976
	ds_read_b128 v[146:149], v237 offset:37056
	ds_read_b128 v[150:153], v237 offset:37072
	v_mfma_f32_32x32x16_bf16 v[18:33], v[38:41], v[170:173], v[18:33]
	ds_read_b128 v[154:157], v237 offset:37088
	ds_read_b128 v[158:161], v237 offset:37104
	ds_read_b128 v[178:181], v236 offset:30208
	v_mfma_f32_32x32x16_bf16 v[18:33], v[34:37], v[174:177], v[18:33]
	ds_read_b128 v[182:185], v236 offset:30240
	ds_read_b128 v[186:189], v236 offset:30272
	ds_read_b128 v[190:193], v236 offset:30304
	s_waitcnt lgkmcnt(0)
	v_mfma_f32_32x32x16_bf16 v[130:145], v[94:97], v[178:181], v[130:145]
	v_mfma_f32_32x32x16_bf16 v[130:145], v[90:93], v[182:185], v[130:145]
	v_mfma_f32_32x32x16_bf16 v[130:145], v[86:89], v[186:189], v[130:145]
	v_mfma_f32_32x32x16_bf16 v[130:145], v[82:85], v[190:193], v[130:145]
	s_nop 7
	v_add_u32_e32 v239, 0x10400, v238
	ds_write_b128 v239, v[2:5] offset:0
	ds_write_b128 v239, v[6:9] offset:16
	ds_write_b128 v239, v[10:13] offset:32
	ds_write_b128 v239, v[14:17] offset:48
	ds_write_b128 v239, v[18:21] offset:128
	ds_write_b128 v239, v[22:25] offset:144
	ds_write_b128 v239, v[26:29] offset:160
	ds_write_b128 v239, v[30:33] offset:176
	v_mfma_f32_32x32x16_bf16 v[146:161], v[46:49], v[178:181], v[146:161]
	v_mfma_f32_32x32x16_bf16 v[146:161], v[42:45], v[182:185], v[146:161]
	v_mfma_f32_32x32x16_bf16 v[146:161], v[38:41], v[186:189], v[146:161]
	v_mfma_f32_32x32x16_bf16 v[146:161], v[34:37], v[190:193], v[146:161]
	s_nop 7
	s_nop 7
	v_cmp_gt_u32_e32 vcc, 16, v228
	s_and_saveexec_b64 s[20:21], vcc
	v_add_u32_e32 v239, 0x18600, v238
	ds_write_b128 v239, v[130:133] offset:0
	ds_write_b128 v239, v[134:137] offset:16
	ds_write_b128 v239, v[138:141] offset:32
	ds_write_b128 v239, v[142:145] offset:48
	ds_write_b128 v239, v[146:149] offset:128
	ds_write_b128 v239, v[150:153] offset:144
	ds_write_b128 v239, v[154:157] offset:160
	ds_write_b128 v239, v[158:161] offset:176
	s_or_b64 exec, exec, s[20:21]
	s_waitcnt vmcnt(0) lgkmcnt(0)
	s_nop 7
	s_nop 7
	s_waitcnt vmcnt(0)
	v_add_u32_e32 v231, s7, v229
	v_add_u32_e32 v231, 0xb840, v231
	v_add_u32_e32 v211, s6, v210
	s_mov_b32 s12, 0x4038aa3b
	v_mov_b32_e32 v235, 0xc038aa3b
	s_nop 0
	s_load_dwordx8 s[4:11], s[0:1], 0x10
	s_waitcnt lgkmcnt(0)
	v_add_u32_e32 v232, 0x24e80, v228
	ds_read_b32 v244, v232
	ds_read_b32 v245, v232 offset:128
	v_mov_b32_e32 v194, 0
	v_mov_b32_e32 v195, 0
	v_mov_b32_e32 v196, 0
	v_mov_b32_e32 v197, 0
	v_mov_b32_e32 v198, 0
	v_mov_b32_e32 v199, 0
	v_mov_b32_e32 v200, 0
	v_mov_b32_e32 v201, 0
	v_mov_b32_e32 v202, 0
	v_mov_b32_e32 v203, 0
	v_mov_b32_e32 v204, 0
	v_mov_b32_e32 v205, 0
	v_mov_b32_e32 v206, 0
	v_mov_b32_e32 v207, 0
	v_mov_b32_e32 v208, 0
	v_mov_b32_e32 v209, 0
	v_add_u32_e32 v232, 0x100, v232
	s_waitcnt lgkmcnt(0)
	v_add_u32_e32 v233, v231, v244
	v_add_u32_e32 v234, v231, v245
	ds_read_b128 v[2:5], v233 offset:0
	ds_read_b128 v[6:9], v233 offset:16
	ds_read_b128 v[10:13], v233 offset:32
	ds_read_b128 v[14:17], v233 offset:48
	ds_read_b128 v[18:21], v233 offset:128
	ds_read_b128 v[22:25], v233 offset:144
	ds_read_b128 v[26:29], v233 offset:160
	ds_read_b128 v[30:33], v233 offset:176
	ds_read_b128 v[34:37], v234 offset:0
	ds_read_b128 v[38:41], v234 offset:16
	ds_read_b128 v[42:45], v234 offset:32
	ds_read_b128 v[46:49], v234 offset:48
	s_movk_i32 s16, 18
	s_waitcnt lgkmcnt(0)
	ds_read_b128 v[82:85], v234 offset:128
	ds_read_b128 v[86:89], v234 offset:144
	ds_read_b128 v[90:93], v234 offset:160
	ds_read_b128 v[94:97], v234 offset:176
	ds_read2_b32 v[244:245], v232 offset1:32
	v_exp_f32_e32 v212, v4
	v_exp_f32_e32 v213, v8
	v_exp_f32_e32 v214, v12
	v_exp_f32_e32 v215, v16
	v_exp_f32_e32 v217, v2
	v_add_f32_e32 v251, 1.0, v212
	v_exp_f32_e32 v218, v6
	v_add_f32_e32 v252, 1.0, v213
	v_exp_f32_e32 v219, v10
	v_add_f32_e32 v253, 1.0, v214
	v_exp_f32_e32 v220, v14
	v_add_f32_e32 v254, 1.0, v215
	v_fma_f32 v240, v212, s12, v235
	v_fma_f32 v241, v213, s12, v235
	v_fma_f32 v242, v214, s12, v235
	v_fma_f32 v243, v215, s12, v235
	v_fmac_f32_e32 v251, v217, v251
	v_fmac_f32_e32 v252, v218, v252
	v_fmac_f32_e32 v253, v219, v253
	v_fmac_f32_e32 v254, v220, v254
	v_rcp_f32_e32 v217, v251
	v_rcp_f32_e32 v218, v252
	v_rcp_f32_e32 v219, v253
	v_rcp_f32_e32 v220, v254
	v_exp_f32_e32 v246, v5
	v_mul_f32_e32 v194, v240, v217
	v_exp_f32_e32 v247, v9
	v_mul_f32_e32 v195, v241, v218
	v_exp_f32_e32 v248, v13
	v_mul_f32_e32 v196, v242, v219
	v_exp_f32_e32 v249, v17
	v_mul_f32_e32 v197, v243, v220
	v_exp_f32_e32 v212, v194
	v_add_f32_e32 v246, 1.0, v246
	v_exp_f32_e32 v213, v195
	v_add_f32_e32 v247, 1.0, v247
	v_exp_f32_e32 v214, v196
	v_add_f32_e32 v248, 1.0, v248
	v_exp_f32_e32 v215, v197
	v_add_f32_e32 v249, 1.0, v249
	v_fmac_f32_e32 v246, v246, v212
	v_fmac_f32_e32 v247, v247, v213
	v_fmac_f32_e32 v248, v248, v214
	v_fmac_f32_e32 v249, v249, v215
	v_rcp_f32_e32 v246, v246
	v_rcp_f32_e32 v247, v247
	v_rcp_f32_e32 v248, v248
	v_rcp_f32_e32 v249, v249
	v_fma_f32 v246, -v212, v246, v246
	v_fma_f32 v247, -v213, v247, v247
	v_fma_f32 v248, -v214, v248, v248
	v_fma_f32 v249, -v215, v249, v249
	v_cvt_pk_bf16_f32 v236, v246, v247
	v_cvt_pk_bf16_f32 v237, v248, v249
	s_waitcnt lgkmcnt(0)
	v_add_u32_e32 v233, v231, v244
	ds_read_b128 v[2:5], v233 offset:0
	ds_read_b128 v[6:9], v233 offset:16
	ds_read_b128 v[10:13], v233 offset:32
	ds_read_b128 v[14:17], v233 offset:48
	v_exp_f32_e32 v212, v20
	v_exp_f32_e32 v213, v24
	v_exp_f32_e32 v214, v28
	v_exp_f32_e32 v215, v32
	v_exp_f32_e32 v217, v18
	v_add_f32_e32 v251, 1.0, v212
	v_exp_f32_e32 v218, v22
	v_add_f32_e32 v252, 1.0, v213
	v_exp_f32_e32 v219, v26
	v_add_f32_e32 v253, 1.0, v214
	v_exp_f32_e32 v220, v30
	v_add_f32_e32 v254, 1.0, v215
	v_fma_f32 v240, v212, s12, v235
	v_fma_f32 v241, v213, s12, v235
	v_fma_f32 v242, v214, s12, v235
	v_fma_f32 v243, v215, s12, v235
	v_fmac_f32_e32 v251, v217, v251
	v_fmac_f32_e32 v252, v218, v252
	v_fmac_f32_e32 v253, v219, v253
	v_fmac_f32_e32 v254, v220, v254
	v_rcp_f32_e32 v217, v251
	v_rcp_f32_e32 v218, v252
	v_rcp_f32_e32 v219, v253
	v_rcp_f32_e32 v220, v254
	v_exp_f32_e32 v246, v21
	v_mul_f32_e32 v198, v240, v217
	v_exp_f32_e32 v247, v25
	v_mul_f32_e32 v199, v241, v218
	v_exp_f32_e32 v248, v29
	v_mul_f32_e32 v200, v242, v219
	v_exp_f32_e32 v249, v33
	v_mul_f32_e32 v201, v243, v220
	v_exp_f32_e32 v212, v198
	v_add_f32_e32 v246, 1.0, v246
	v_exp_f32_e32 v213, v199
	v_add_f32_e32 v247, 1.0, v247
	v_exp_f32_e32 v214, v200
	v_add_f32_e32 v248, 1.0, v248
	v_exp_f32_e32 v215, v201
	v_add_f32_e32 v249, 1.0, v249
	v_fmac_f32_e32 v246, v246, v212
	v_fmac_f32_e32 v247, v247, v213
	v_fmac_f32_e32 v248, v248, v214
	v_fmac_f32_e32 v249, v249, v215
	v_rcp_f32_e32 v246, v246
	v_rcp_f32_e32 v247, v247
	v_rcp_f32_e32 v248, v248
	v_rcp_f32_e32 v249, v249
	v_fma_f32 v246, -v212, v246, v246
	v_fma_f32 v247, -v213, v247, v247
	v_fma_f32 v248, -v214, v248, v248
	v_fma_f32 v249, -v215, v249, v249
	v_cvt_pk_bf16_f32 v238, v246, v247
	v_cvt_pk_bf16_f32 v239, v248, v249
	ds_write_b128 v211, v[236:239] offset:0
	s_waitcnt lgkmcnt(0)
	s_barrier
	ds_read_b128 v[130:133], v210 offset:0
	ds_read_b128 v[134:137], v210 offset:1024
	ds_read_b128 v[18:21], v233 offset:128
	ds_read_b128 v[22:25], v233 offset:144
	ds_read_b128 v[26:29], v233 offset:160
	ds_read_b128 v[30:33], v233 offset:176
	v_exp_f32_e32 v212, v36
	v_exp_f32_e32 v213, v40
	v_exp_f32_e32 v214, v44
	v_exp_f32_e32 v215, v48
	ds_read_b128 v[138:141], v210 offset:2048
	ds_read_b128 v[142:145], v210 offset:3072
	v_exp_f32_e32 v217, v34
	v_add_f32_e32 v251, 1.0, v212
	v_exp_f32_e32 v218, v38
	v_add_f32_e32 v252, 1.0, v213
	v_exp_f32_e32 v219, v42
	v_add_f32_e32 v253, 1.0, v214
	v_exp_f32_e32 v220, v46
	v_add_f32_e32 v254, 1.0, v215
	v_fma_f32 v240, v212, s12, v235
	v_fma_f32 v241, v213, s12, v235
	v_fma_f32 v242, v214, s12, v235
	v_fma_f32 v243, v215, s12, v235
	ds_read_b128 v[146:149], v210 offset:4096
	ds_read_b128 v[150:153], v210 offset:5120
	v_fmac_f32_e32 v251, v217, v251
	v_fmac_f32_e32 v252, v218, v252
	v_fmac_f32_e32 v253, v219, v253
	v_fmac_f32_e32 v254, v220, v254
	ds_read_b128 v[154:157], v210 offset:6144
	ds_read_b128 v[158:161], v210 offset:7168
	v_rcp_f32_e32 v217, v251
	v_rcp_f32_e32 v218, v252
	v_rcp_f32_e32 v219, v253
	v_rcp_f32_e32 v220, v254
	v_exp_f32_e32 v246, v37
	v_mul_f32_e32 v202, v240, v217
	v_exp_f32_e32 v247, v41
	v_mul_f32_e32 v203, v241, v218
	v_exp_f32_e32 v248, v45
	v_mul_f32_e32 v204, v242, v219
	v_exp_f32_e32 v249, v49
	v_mul_f32_e32 v205, v243, v220
	v_exp_f32_e32 v212, v202
	v_add_f32_e32 v246, 1.0, v246
	v_exp_f32_e32 v213, v203
	v_add_f32_e32 v247, 1.0, v247
	v_exp_f32_e32 v214, v204
	v_add_f32_e32 v248, 1.0, v248
	v_exp_f32_e32 v215, v205
	v_add_f32_e32 v249, 1.0, v249
	v_fmac_f32_e32 v246, v246, v212
	v_fmac_f32_e32 v247, v247, v213
	v_fmac_f32_e32 v248, v248, v214
	v_fmac_f32_e32 v249, v249, v215
	v_rcp_f32_e32 v246, v246
	v_rcp_f32_e32 v247, v247
	v_rcp_f32_e32 v248, v248
	v_rcp_f32_e32 v249, v249
	v_fma_f32 v246, -v212, v246, v246
	v_fma_f32 v247, -v213, v247, v247
	v_fma_f32 v248, -v214, v248, v248
	v_fma_f32 v249, -v215, v249, v249
	v_cvt_pk_bf16_f32 v236, v246, v247
	v_cvt_pk_bf16_f32 v237, v248, v249
	s_waitcnt lgkmcnt(0)
	v_mfma_f32_32x32x16_bf16 v[2:17], v[126:129], v[130:133], v[2:17]
	v_add_u32_e32 v234, v231, v245
	ds_read_b128 v[34:37], v234 offset:0
	ds_read_b128 v[38:41], v234 offset:16
	ds_read_b128 v[42:45], v234 offset:32
	ds_read_b128 v[46:49], v234 offset:48
	v_add_u32_e32 v232, 0x100, v232
	v_exp_f32_e32 v212, v84
	v_exp_f32_e32 v213, v88
	v_exp_f32_e32 v214, v92
	v_exp_f32_e32 v215, v96
	v_mfma_f32_32x32x16_bf16 v[2:17], v[122:125], v[134:137], v[2:17]
	v_exp_f32_e32 v217, v82
	v_add_f32_e32 v251, 1.0, v212
	v_exp_f32_e32 v218, v86
	v_add_f32_e32 v252, 1.0, v213
	v_exp_f32_e32 v219, v90
	v_add_f32_e32 v253, 1.0, v214
	v_exp_f32_e32 v220, v94
	v_add_f32_e32 v254, 1.0, v215
	v_fma_f32 v240, v212, s12, v235
	v_fma_f32 v241, v213, s12, v235
	v_fma_f32 v242, v214, s12, v235
	v_fma_f32 v243, v215, s12, v235
	v_mfma_f32_32x32x16_bf16 v[2:17], v[118:121], v[138:141], v[2:17]
	v_fmac_f32_e32 v251, v217, v251
	v_fmac_f32_e32 v252, v218, v252
	v_fmac_f32_e32 v253, v219, v253
	v_fmac_f32_e32 v254, v220, v254
	v_mfma_f32_32x32x16_bf16 v[2:17], v[114:117], v[142:145], v[2:17]
	v_rcp_f32_e32 v217, v251
	v_rcp_f32_e32 v218, v252
	v_rcp_f32_e32 v219, v253
	v_rcp_f32_e32 v220, v254
	v_mfma_f32_32x32x16_bf16 v[2:17], v[110:113], v[146:149], v[2:17]
	v_exp_f32_e32 v246, v85
	v_mul_f32_e32 v206, v240, v217
	v_exp_f32_e32 v247, v89
	v_mul_f32_e32 v207, v241, v218
	v_exp_f32_e32 v248, v93
	v_mul_f32_e32 v208, v242, v219
	v_exp_f32_e32 v249, v97
	v_mul_f32_e32 v209, v243, v220
	v_mfma_f32_32x32x16_bf16 v[2:17], v[106:109], v[150:153], v[2:17]
	v_mfma_f32_32x32x16_bf16 v[2:17], v[102:105], v[154:157], v[2:17]
	v_exp_f32_e32 v212, v206
	v_add_f32_e32 v246, 1.0, v246
	v_exp_f32_e32 v213, v207
	v_add_f32_e32 v247, 1.0, v247
	v_exp_f32_e32 v214, v208
	v_add_f32_e32 v248, 1.0, v248
	v_exp_f32_e32 v215, v209
	v_add_f32_e32 v249, 1.0, v249
	v_fmac_f32_e32 v246, v246, v212
	v_fmac_f32_e32 v247, v247, v213
	v_fmac_f32_e32 v248, v248, v214
	v_fmac_f32_e32 v249, v249, v215
	v_mfma_f32_32x32x16_bf16 v[2:17], v[98:101], v[158:161], v[2:17]
	v_rcp_f32_e32 v246, v246
	v_rcp_f32_e32 v247, v247
	v_rcp_f32_e32 v248, v248
	v_rcp_f32_e32 v249, v249
	v_fma_f32 v246, -v212, v246, v246
	v_fma_f32 v247, -v213, v247, v247
	v_fma_f32 v248, -v214, v248, v248
	v_fma_f32 v249, -v215, v249, v249
	v_cvt_pk_bf16_f32 v238, v246, v247
	v_cvt_pk_bf16_f32 v239, v248, v249
	ds_write_b128 v211, v[236:239] offset:8192
	s_waitcnt lgkmcnt(0)
	s_barrier
	.p2align 6
.Llight_loop:
	v_mfma_f32_32x32x16_bf16 v[18:33], v[78:81], v[130:133], v[18:33]
	ds_read_b128 v[162:165], v210 offset:8192
	ds_read_b128 v[166:169], v210 offset:9216
	ds_read_b128 v[82:85], v234 offset:128
	ds_read_b128 v[86:89], v234 offset:144
	ds_read_b128 v[90:93], v234 offset:160
	ds_read_b128 v[94:97], v234 offset:176
	ds_read2_b32 v[244:245], v232 offset1:32
	v_exp_f32_e32 v212, v4
	v_exp_f32_e32 v213, v8
	v_exp_f32_e32 v214, v12
	v_exp_f32_e32 v215, v16
	v_mfma_f32_32x32x16_bf16 v[18:33], v[74:77], v[134:137], v[18:33]
	ds_read_b128 v[170:173], v210 offset:10240
	ds_read_b128 v[174:177], v210 offset:11264
	v_exp_f32_e32 v217, v2
	v_add_f32_e32 v251, 1.0, v212
	v_exp_f32_e32 v218, v6
	v_add_f32_e32 v252, 1.0, v213
	v_exp_f32_e32 v219, v10
	v_add_f32_e32 v253, 1.0, v214
	v_exp_f32_e32 v220, v14
	v_add_f32_e32 v254, 1.0, v215
	v_fma_f32 v240, v212, s12, v235
	v_fma_f32 v241, v213, s12, v235
	v_fma_f32 v242, v214, s12, v235
	v_fma_f32 v243, v215, s12, v235
	v_mfma_f32_32x32x16_bf16 v[18:33], v[70:73], v[138:141], v[18:33]
	ds_read_b128 v[178:181], v210 offset:12288
	ds_read_b128 v[182:185], v210 offset:13312
	v_exp_f32_e32 v221, v3
	v_fmac_f32_e32 v251, v217, v251
	v_exp_f32_e32 v222, v7
	v_fmac_f32_e32 v252, v218, v252
	v_exp_f32_e32 v223, v11
	v_fmac_f32_e32 v253, v219, v253
	v_exp_f32_e32 v224, v15
	v_fmac_f32_e32 v254, v220, v254
	v_mfma_f32_32x32x16_bf16 v[18:33], v[66:69], v[142:145], v[18:33]
	ds_read_b128 v[186:189], v210 offset:14336
	ds_read_b128 v[190:193], v210 offset:15360
	v_rcp_f32_e32 v217, v251
	v_add_f32_e32 v221, 1.0, v221
	v_rcp_f32_e32 v218, v252
	v_add_f32_e32 v222, 1.0, v222
	v_rcp_f32_e32 v219, v253
	v_add_f32_e32 v223, 1.0, v223
	v_rcp_f32_e32 v220, v254
	v_add_f32_e32 v224, 1.0, v224
	v_mfma_f32_32x32x16_bf16 v[18:33], v[62:65], v[146:149], v[18:33]
	v_rcp_f32_e32 v221, v221
	v_mul_f32_e32 v240, v240, v217
	v_rcp_f32_e32 v222, v222
	v_mul_f32_e32 v241, v241, v218
	v_rcp_f32_e32 v223, v223
	v_mul_f32_e32 v242, v242, v219
	v_rcp_f32_e32 v224, v224
	v_mul_f32_e32 v243, v243, v220
	v_mfma_f32_32x32x16_bf16 v[18:33], v[58:61], v[150:153], v[18:33]
	v_exp_f32_e32 v246, v5
	v_fma_f32 v194, v221, v194, v240
	v_exp_f32_e32 v247, v9
	v_fma_f32 v195, v222, v195, v241
	v_exp_f32_e32 v248, v13
	v_fma_f32 v196, v223, v196, v242
	v_exp_f32_e32 v249, v17
	v_fma_f32 v197, v224, v197, v243
	v_mfma_f32_32x32x16_bf16 v[18:33], v[54:57], v[154:157], v[18:33]
	v_exp_f32_e32 v212, v194
	v_add_f32_e32 v246, 1.0, v246
	v_exp_f32_e32 v213, v195
	v_add_f32_e32 v247, 1.0, v247
	v_exp_f32_e32 v214, v196
	v_add_f32_e32 v248, 1.0, v248
	v_exp_f32_e32 v215, v197
	v_add_f32_e32 v249, 1.0, v249
	v_fmac_f32_e32 v246, v246, v212
	v_fmac_f32_e32 v247, v247, v213
	v_fmac_f32_e32 v248, v248, v214
	v_fmac_f32_e32 v249, v249, v215
	v_mfma_f32_32x32x16_bf16 v[18:33], v[50:53], v[158:161], v[18:33]
	v_rcp_f32_e32 v246, v246
	v_rcp_f32_e32 v247, v247
	v_rcp_f32_e32 v248, v248
	v_rcp_f32_e32 v249, v249
	v_fma_f32 v246, -v212, v246, v246
	v_fma_f32 v247, -v213, v247, v247
	v_fma_f32 v248, -v214, v248, v248
	v_fma_f32 v249, -v215, v249, v249
	v_cvt_pk_bf16_f32 v236, v246, v247
	v_cvt_pk_bf16_f32 v237, v248, v249
	s_waitcnt lgkmcnt(0)
	v_mfma_f32_32x32x16_bf16 v[34:49], v[126:129], v[162:165], v[34:49]
	v_add_u32_e32 v233, v231, v244
	ds_read_b128 v[2:5], v233 offset:0
	ds_read_b128 v[6:9], v233 offset:16
	ds_read_b128 v[10:13], v233 offset:32
	ds_read_b128 v[14:17], v233 offset:48
	v_exp_f32_e32 v212, v20
	v_exp_f32_e32 v213, v24
	v_exp_f32_e32 v214, v28
	v_exp_f32_e32 v215, v32
	v_mfma_f32_32x32x16_bf16 v[34:49], v[122:125], v[166:169], v[34:49]
	v_exp_f32_e32 v217, v18
	v_add_f32_e32 v251, 1.0, v212
	v_exp_f32_e32 v218, v22
	v_add_f32_e32 v252, 1.0, v213
	v_exp_f32_e32 v219, v26
	v_add_f32_e32 v253, 1.0, v214
	v_exp_f32_e32 v220, v30
	v_add_f32_e32 v254, 1.0, v215
	v_fma_f32 v240, v212, s12, v235
	v_fma_f32 v241, v213, s12, v235
	v_fma_f32 v242, v214, s12, v235
	v_fma_f32 v243, v215, s12, v235
	v_mfma_f32_32x32x16_bf16 v[34:49], v[118:121], v[170:173], v[34:49]
	v_exp_f32_e32 v221, v19
	v_fmac_f32_e32 v251, v217, v251
	v_exp_f32_e32 v222, v23
	v_fmac_f32_e32 v252, v218, v252
	v_exp_f32_e32 v223, v27
	v_fmac_f32_e32 v253, v219, v253
	v_exp_f32_e32 v224, v31
	v_fmac_f32_e32 v254, v220, v254
	v_mfma_f32_32x32x16_bf16 v[34:49], v[114:117], v[174:177], v[34:49]
	v_rcp_f32_e32 v217, v251
	v_add_f32_e32 v221, 1.0, v221
	v_rcp_f32_e32 v218, v252
	v_add_f32_e32 v222, 1.0, v222
	v_rcp_f32_e32 v219, v253
	v_add_f32_e32 v223, 1.0, v223
	v_rcp_f32_e32 v220, v254
	v_add_f32_e32 v224, 1.0, v224
	v_mfma_f32_32x32x16_bf16 v[34:49], v[110:113], v[178:181], v[34:49]
	v_rcp_f32_e32 v221, v221
	v_mul_f32_e32 v240, v240, v217
	v_rcp_f32_e32 v222, v222
	v_mul_f32_e32 v241, v241, v218
	v_rcp_f32_e32 v223, v223
	v_mul_f32_e32 v242, v242, v219
	v_rcp_f32_e32 v224, v224
	v_mul_f32_e32 v243, v243, v220
	v_mfma_f32_32x32x16_bf16 v[34:49], v[106:109], v[182:185], v[34:49]
	v_exp_f32_e32 v246, v21
	v_fma_f32 v198, v221, v198, v240
	v_exp_f32_e32 v247, v25
	v_fma_f32 v199, v222, v199, v241
	v_exp_f32_e32 v248, v29
	v_fma_f32 v200, v223, v200, v242
	v_exp_f32_e32 v249, v33
	v_fma_f32 v201, v224, v201, v243
	v_mfma_f32_32x32x16_bf16 v[34:49], v[102:105], v[186:189], v[34:49]
	v_exp_f32_e32 v212, v198
	v_add_f32_e32 v246, 1.0, v246
	v_exp_f32_e32 v213, v199
	v_add_f32_e32 v247, 1.0, v247
	v_exp_f32_e32 v214, v200
	v_add_f32_e32 v248, 1.0, v248
	v_exp_f32_e32 v215, v201
	v_add_f32_e32 v249, 1.0, v249
	v_fmac_f32_e32 v246, v246, v212
	v_fmac_f32_e32 v247, v247, v213
	v_fmac_f32_e32 v248, v248, v214
	v_fmac_f32_e32 v249, v249, v215
	v_mfma_f32_32x32x16_bf16 v[34:49], v[98:101], v[190:193], v[34:49]
	v_rcp_f32_e32 v246, v246
	v_rcp_f32_e32 v247, v247
	v_rcp_f32_e32 v248, v248
	v_rcp_f32_e32 v249, v249
	v_fma_f32 v246, -v212, v246, v246
	v_fma_f32 v247, -v213, v247, v247
	v_fma_f32 v248, -v214, v248, v248
	v_fma_f32 v249, -v215, v249, v249
	v_cvt_pk_bf16_f32 v238, v246, v247
	v_cvt_pk_bf16_f32 v239, v248, v249
	ds_write_b128 v211, v[236:239] offset:0
	s_waitcnt lgkmcnt(0)
	s_barrier
	v_mfma_f32_32x32x16_bf16 v[82:97], v[78:81], v[162:165], v[82:97]
	ds_read_b128 v[130:133], v210 offset:0
	ds_read_b128 v[134:137], v210 offset:1024
	ds_read_b128 v[18:21], v233 offset:128
	ds_read_b128 v[22:25], v233 offset:144
	ds_read_b128 v[26:29], v233 offset:160
	ds_read_b128 v[30:33], v233 offset:176
	v_exp_f32_e32 v212, v36
	v_exp_f32_e32 v213, v40
	v_exp_f32_e32 v214, v44
	v_exp_f32_e32 v215, v48
	v_mfma_f32_32x32x16_bf16 v[82:97], v[74:77], v[166:169], v[82:97]
	ds_read_b128 v[138:141], v210 offset:2048
	ds_read_b128 v[142:145], v210 offset:3072
	v_exp_f32_e32 v217, v34
	v_add_f32_e32 v251, 1.0, v212
	v_exp_f32_e32 v218, v38
	v_add_f32_e32 v252, 1.0, v213
	v_exp_f32_e32 v219, v42
	v_add_f32_e32 v253, 1.0, v214
	v_exp_f32_e32 v220, v46
	v_add_f32_e32 v254, 1.0, v215
	v_fma_f32 v240, v212, s12, v235
	v_fma_f32 v241, v213, s12, v235
	v_fma_f32 v242, v214, s12, v235
	v_fma_f32 v243, v215, s12, v235
	v_mfma_f32_32x32x16_bf16 v[82:97], v[70:73], v[170:173], v[82:97]
	ds_read_b128 v[146:149], v210 offset:4096
	ds_read_b128 v[150:153], v210 offset:5120
	v_exp_f32_e32 v221, v35
	v_fmac_f32_e32 v251, v217, v251
	v_exp_f32_e32 v222, v39
	v_fmac_f32_e32 v252, v218, v252
	v_exp_f32_e32 v223, v43
	v_fmac_f32_e32 v253, v219, v253
	v_exp_f32_e32 v224, v47
	v_fmac_f32_e32 v254, v220, v254
	v_mfma_f32_32x32x16_bf16 v[82:97], v[66:69], v[174:177], v[82:97]
	ds_read_b128 v[154:157], v210 offset:6144
	ds_read_b128 v[158:161], v210 offset:7168
	v_rcp_f32_e32 v217, v251
	v_add_f32_e32 v221, 1.0, v221
	v_rcp_f32_e32 v218, v252
	v_add_f32_e32 v222, 1.0, v222
	v_rcp_f32_e32 v219, v253
	v_add_f32_e32 v223, 1.0, v223
	v_rcp_f32_e32 v220, v254
	v_add_f32_e32 v224, 1.0, v224
	v_mfma_f32_32x32x16_bf16 v[82:97], v[62:65], v[178:181], v[82:97]
	v_rcp_f32_e32 v221, v221
	v_mul_f32_e32 v240, v240, v217
	v_rcp_f32_e32 v222, v222
	v_mul_f32_e32 v241, v241, v218
	v_rcp_f32_e32 v223, v223
	v_mul_f32_e32 v242, v242, v219
	v_rcp_f32_e32 v224, v224
	v_mul_f32_e32 v243, v243, v220
	v_mfma_f32_32x32x16_bf16 v[82:97], v[58:61], v[182:185], v[82:97]
	v_exp_f32_e32 v246, v37
	v_fma_f32 v202, v221, v202, v240
	v_exp_f32_e32 v247, v41
	v_fma_f32 v203, v222, v203, v241
	v_exp_f32_e32 v248, v45
	v_fma_f32 v204, v223, v204, v242
	v_exp_f32_e32 v249, v49
	v_fma_f32 v205, v224, v205, v243
	v_mfma_f32_32x32x16_bf16 v[82:97], v[54:57], v[186:189], v[82:97]
	v_exp_f32_e32 v212, v202
	v_add_f32_e32 v246, 1.0, v246
	v_exp_f32_e32 v213, v203
	v_add_f32_e32 v247, 1.0, v247
	v_exp_f32_e32 v214, v204
	v_add_f32_e32 v248, 1.0, v248
	v_exp_f32_e32 v215, v205
	v_add_f32_e32 v249, 1.0, v249
	v_fmac_f32_e32 v246, v246, v212
	v_fmac_f32_e32 v247, v247, v213
	v_fmac_f32_e32 v248, v248, v214
	v_fmac_f32_e32 v249, v249, v215
	v_mfma_f32_32x32x16_bf16 v[82:97], v[50:53], v[190:193], v[82:97]
	v_rcp_f32_e32 v246, v246
	v_rcp_f32_e32 v247, v247
	v_rcp_f32_e32 v248, v248
	v_rcp_f32_e32 v249, v249
	v_fma_f32 v246, -v212, v246, v246
	v_fma_f32 v247, -v213, v247, v247
	v_fma_f32 v248, -v214, v248, v248
	v_fma_f32 v249, -v215, v249, v249
	v_cvt_pk_bf16_f32 v236, v246, v247
	v_cvt_pk_bf16_f32 v237, v248, v249
	s_waitcnt lgkmcnt(0)
	v_mfma_f32_32x32x16_bf16 v[2:17], v[126:129], v[130:133], v[2:17]
	v_add_u32_e32 v234, v231, v245
	ds_read_b128 v[34:37], v234 offset:0
	ds_read_b128 v[38:41], v234 offset:16
	ds_read_b128 v[42:45], v234 offset:32
	ds_read_b128 v[46:49], v234 offset:48
	v_add_u32_e32 v232, 0x100, v232
	v_exp_f32_e32 v212, v84
	v_exp_f32_e32 v213, v88
	v_exp_f32_e32 v214, v92
	v_exp_f32_e32 v215, v96
	v_mfma_f32_32x32x16_bf16 v[2:17], v[122:125], v[134:137], v[2:17]
	v_exp_f32_e32 v217, v82
	v_add_f32_e32 v251, 1.0, v212
	v_exp_f32_e32 v218, v86
	v_add_f32_e32 v252, 1.0, v213
	v_exp_f32_e32 v219, v90
	v_add_f32_e32 v253, 1.0, v214
	v_exp_f32_e32 v220, v94
	v_add_f32_e32 v254, 1.0, v215
	v_fma_f32 v240, v212, s12, v235
	v_fma_f32 v241, v213, s12, v235
	v_fma_f32 v242, v214, s12, v235
	v_fma_f32 v243, v215, s12, v235
	v_mfma_f32_32x32x16_bf16 v[2:17], v[118:121], v[138:141], v[2:17]
	v_exp_f32_e32 v221, v83
	v_fmac_f32_e32 v251, v217, v251
	v_exp_f32_e32 v222, v87
	v_fmac_f32_e32 v252, v218, v252
	v_exp_f32_e32 v223, v91
	v_fmac_f32_e32 v253, v219, v253
	v_exp_f32_e32 v224, v95
	v_fmac_f32_e32 v254, v220, v254
	v_mfma_f32_32x32x16_bf16 v[2:17], v[114:117], v[142:145], v[2:17]
	v_rcp_f32_e32 v217, v251
	v_add_f32_e32 v221, 1.0, v221
	v_rcp_f32_e32 v218, v252
	v_add_f32_e32 v222, 1.0, v222
	v_rcp_f32_e32 v219, v253
	v_add_f32_e32 v223, 1.0, v223
	v_rcp_f32_e32 v220, v254
	v_add_f32_e32 v224, 1.0, v224
	v_mfma_f32_32x32x16_bf16 v[2:17], v[110:113], v[146:149], v[2:17]
	v_rcp_f32_e32 v221, v221
	v_mul_f32_e32 v240, v240, v217
	v_rcp_f32_e32 v222, v222
	v_mul_f32_e32 v241, v241, v218
	v_rcp_f32_e32 v223, v223
	v_mul_f32_e32 v242, v242, v219
	v_rcp_f32_e32 v224, v224
	v_mul_f32_e32 v243, v243, v220
	v_mfma_f32_32x32x16_bf16 v[2:17], v[106:109], v[150:153], v[2:17]
	v_exp_f32_e32 v246, v85
	v_fma_f32 v206, v221, v206, v240
	v_exp_f32_e32 v247, v89
	v_fma_f32 v207, v222, v207, v241
	v_exp_f32_e32 v248, v93
	v_fma_f32 v208, v223, v208, v242
	v_exp_f32_e32 v249, v97
	v_fma_f32 v209, v224, v209, v243
	v_mfma_f32_32x32x16_bf16 v[2:17], v[102:105], v[154:157], v[2:17]
	v_exp_f32_e32 v212, v206
	v_add_f32_e32 v246, 1.0, v246
	v_exp_f32_e32 v213, v207
	v_add_f32_e32 v247, 1.0, v247
	v_exp_f32_e32 v214, v208
	v_add_f32_e32 v248, 1.0, v248
	v_exp_f32_e32 v215, v209
	v_add_f32_e32 v249, 1.0, v249
	v_fmac_f32_e32 v246, v246, v212
	v_fmac_f32_e32 v247, v247, v213
	v_fmac_f32_e32 v248, v248, v214
	v_fmac_f32_e32 v249, v249, v215
	v_mfma_f32_32x32x16_bf16 v[2:17], v[98:101], v[158:161], v[2:17]
	v_rcp_f32_e32 v246, v246
	v_rcp_f32_e32 v247, v247
	v_rcp_f32_e32 v248, v248
	v_rcp_f32_e32 v249, v249
	v_fma_f32 v246, -v212, v246, v246
	v_fma_f32 v247, -v213, v247, v247
	v_fma_f32 v248, -v214, v248, v248
	v_fma_f32 v249, -v215, v249, v249
	v_cvt_pk_bf16_f32 v238, v246, v247
	v_cvt_pk_bf16_f32 v239, v248, v249
	ds_write_b128 v211, v[236:239] offset:8192
	s_waitcnt lgkmcnt(0)
	s_barrier
	s_sub_u32 s16, s16, 1
	s_cmp_lg_u32 s16, 0
	s_cbranch_scc1 .Llight_loop
	v_mfma_f32_32x32x16_bf16 v[18:33], v[78:81], v[130:133], v[18:33]
	ds_read_b128 v[162:165], v210 offset:8192
	ds_read_b128 v[166:169], v210 offset:9216
	ds_read_b128 v[82:85], v234 offset:128
	ds_read_b128 v[86:89], v234 offset:144
	ds_read_b128 v[90:93], v234 offset:160
	ds_read_b128 v[94:97], v234 offset:176
	v_exp_f32_e32 v212, v4
	v_exp_f32_e32 v213, v8
	v_exp_f32_e32 v214, v12
	v_exp_f32_e32 v215, v16
	v_mfma_f32_32x32x16_bf16 v[18:33], v[74:77], v[134:137], v[18:33]
	ds_read_b128 v[170:173], v210 offset:10240
	ds_read_b128 v[174:177], v210 offset:11264
	v_exp_f32_e32 v217, v2
	v_add_f32_e32 v251, 1.0, v212
	v_exp_f32_e32 v218, v6
	v_add_f32_e32 v252, 1.0, v213
	v_exp_f32_e32 v219, v10
	v_add_f32_e32 v253, 1.0, v214
	v_exp_f32_e32 v220, v14
	v_add_f32_e32 v254, 1.0, v215
	v_fma_f32 v240, v212, s12, v235
	v_fma_f32 v241, v213, s12, v235
	v_fma_f32 v242, v214, s12, v235
	v_fma_f32 v243, v215, s12, v235
	v_mfma_f32_32x32x16_bf16 v[18:33], v[70:73], v[138:141], v[18:33]
	ds_read_b128 v[178:181], v210 offset:12288
	ds_read_b128 v[182:185], v210 offset:13312
	v_exp_f32_e32 v221, v3
	v_fmac_f32_e32 v251, v217, v251
	v_exp_f32_e32 v222, v7
	v_fmac_f32_e32 v252, v218, v252
	v_exp_f32_e32 v223, v11
	v_fmac_f32_e32 v253, v219, v253
	v_exp_f32_e32 v224, v15
	v_fmac_f32_e32 v254, v220, v254
	v_mfma_f32_32x32x16_bf16 v[18:33], v[66:69], v[142:145], v[18:33]
	ds_read_b128 v[186:189], v210 offset:14336
	ds_read_b128 v[190:193], v210 offset:15360
	v_rcp_f32_e32 v217, v251
	v_add_f32_e32 v221, 1.0, v221
	v_rcp_f32_e32 v218, v252
	v_add_f32_e32 v222, 1.0, v222
	v_rcp_f32_e32 v219, v253
	v_add_f32_e32 v223, 1.0, v223
	v_rcp_f32_e32 v220, v254
	v_add_f32_e32 v224, 1.0, v224
	v_mfma_f32_32x32x16_bf16 v[18:33], v[62:65], v[146:149], v[18:33]
	v_rcp_f32_e32 v221, v221
	v_mul_f32_e32 v240, v240, v217
	v_rcp_f32_e32 v222, v222
	v_mul_f32_e32 v241, v241, v218
	v_rcp_f32_e32 v223, v223
	v_mul_f32_e32 v242, v242, v219
	v_rcp_f32_e32 v224, v224
	v_mul_f32_e32 v243, v243, v220
	v_mfma_f32_32x32x16_bf16 v[18:33], v[58:61], v[150:153], v[18:33]
	v_exp_f32_e32 v246, v5
	v_fma_f32 v194, v221, v194, v240
	v_exp_f32_e32 v247, v9
	v_fma_f32 v195, v222, v195, v241
	v_exp_f32_e32 v248, v13
	v_fma_f32 v196, v223, v196, v242
	v_exp_f32_e32 v249, v17
	v_fma_f32 v197, v224, v197, v243
	v_mfma_f32_32x32x16_bf16 v[18:33], v[54:57], v[154:157], v[18:33]
	v_exp_f32_e32 v212, v194
	v_add_f32_e32 v246, 1.0, v246
	v_exp_f32_e32 v213, v195
	v_add_f32_e32 v247, 1.0, v247
	v_exp_f32_e32 v214, v196
	v_add_f32_e32 v248, 1.0, v248
	v_exp_f32_e32 v215, v197
	v_add_f32_e32 v249, 1.0, v249
	v_fmac_f32_e32 v246, v246, v212
	v_fmac_f32_e32 v247, v247, v213
	v_fmac_f32_e32 v248, v248, v214
	v_fmac_f32_e32 v249, v249, v215
	v_mfma_f32_32x32x16_bf16 v[18:33], v[50:53], v[158:161], v[18:33]
	v_rcp_f32_e32 v246, v246
	v_rcp_f32_e32 v247, v247
	v_rcp_f32_e32 v248, v248
	v_rcp_f32_e32 v249, v249
	v_fma_f32 v246, -v212, v246, v246
	v_fma_f32 v247, -v213, v247, v247
	v_fma_f32 v248, -v214, v248, v248
	v_fma_f32 v249, -v215, v249, v249
	v_cvt_pk_bf16_f32 v236, v246, v247
	v_cvt_pk_bf16_f32 v237, v248, v249
	s_waitcnt lgkmcnt(0)
	v_mfma_f32_32x32x16_bf16 v[34:49], v[126:129], v[162:165], v[34:49]
	v_exp_f32_e32 v212, v20
	v_exp_f32_e32 v213, v24
	v_exp_f32_e32 v214, v28
	v_exp_f32_e32 v215, v32
	v_mfma_f32_32x32x16_bf16 v[34:49], v[122:125], v[166:169], v[34:49]
	v_exp_f32_e32 v217, v18
	v_add_f32_e32 v251, 1.0, v212
	v_exp_f32_e32 v218, v22
	v_add_f32_e32 v252, 1.0, v213
	v_exp_f32_e32 v219, v26
	v_add_f32_e32 v253, 1.0, v214
	v_exp_f32_e32 v220, v30
	v_add_f32_e32 v254, 1.0, v215
	v_fma_f32 v240, v212, s12, v235
	v_fma_f32 v241, v213, s12, v235
	v_fma_f32 v242, v214, s12, v235
	v_fma_f32 v243, v215, s12, v235
	v_mfma_f32_32x32x16_bf16 v[34:49], v[118:121], v[170:173], v[34:49]
	v_exp_f32_e32 v221, v19
	v_fmac_f32_e32 v251, v217, v251
	v_exp_f32_e32 v222, v23
	v_fmac_f32_e32 v252, v218, v252
	v_exp_f32_e32 v223, v27
	v_fmac_f32_e32 v253, v219, v253
	v_exp_f32_e32 v224, v31
	v_fmac_f32_e32 v254, v220, v254
	v_mfma_f32_32x32x16_bf16 v[34:49], v[114:117], v[174:177], v[34:49]
	v_rcp_f32_e32 v217, v251
	v_add_f32_e32 v221, 1.0, v221
	v_rcp_f32_e32 v218, v252
	v_add_f32_e32 v222, 1.0, v222
	v_rcp_f32_e32 v219, v253
	v_add_f32_e32 v223, 1.0, v223
	v_rcp_f32_e32 v220, v254
	v_add_f32_e32 v224, 1.0, v224
	v_mfma_f32_32x32x16_bf16 v[34:49], v[110:113], v[178:181], v[34:49]
	v_rcp_f32_e32 v221, v221
	v_mul_f32_e32 v240, v240, v217
	v_rcp_f32_e32 v222, v222
	v_mul_f32_e32 v241, v241, v218
	v_rcp_f32_e32 v223, v223
	v_mul_f32_e32 v242, v242, v219
	v_rcp_f32_e32 v224, v224
	v_mul_f32_e32 v243, v243, v220
	v_mfma_f32_32x32x16_bf16 v[34:49], v[106:109], v[182:185], v[34:49]
	v_exp_f32_e32 v246, v21
	v_fma_f32 v198, v221, v198, v240
	v_exp_f32_e32 v247, v25
	v_fma_f32 v199, v222, v199, v241
	v_exp_f32_e32 v248, v29
	v_fma_f32 v200, v223, v200, v242
	v_exp_f32_e32 v249, v33
	v_fma_f32 v201, v224, v201, v243
	v_mfma_f32_32x32x16_bf16 v[34:49], v[102:105], v[186:189], v[34:49]
	v_exp_f32_e32 v212, v198
	v_add_f32_e32 v246, 1.0, v246
	v_exp_f32_e32 v213, v199
	v_add_f32_e32 v247, 1.0, v247
	v_exp_f32_e32 v214, v200
	v_add_f32_e32 v248, 1.0, v248
	v_exp_f32_e32 v215, v201
	v_add_f32_e32 v249, 1.0, v249
	v_fmac_f32_e32 v246, v246, v212
	v_fmac_f32_e32 v247, v247, v213
	v_fmac_f32_e32 v248, v248, v214
	v_fmac_f32_e32 v249, v249, v215
	v_mfma_f32_32x32x16_bf16 v[34:49], v[98:101], v[190:193], v[34:49]
	v_rcp_f32_e32 v246, v246
	v_rcp_f32_e32 v247, v247
	v_rcp_f32_e32 v248, v248
	v_rcp_f32_e32 v249, v249
	v_fma_f32 v246, -v212, v246, v246
	v_fma_f32 v247, -v213, v247, v247
	v_fma_f32 v248, -v214, v248, v248
	v_fma_f32 v249, -v215, v249, v249
	v_cvt_pk_bf16_f32 v238, v246, v247
	v_cvt_pk_bf16_f32 v239, v248, v249
	ds_write_b128 v211, v[236:239] offset:0
	s_waitcnt lgkmcnt(0)
	s_barrier
	s_bfe_u32 s20, s19, 0x10006
	s_lshl_b32 s21, s20, 7
	s_lshl_b32 s20, s20, 13
	s_add_u32 s20, s20, 0x30000
	s_add_u32 s22, s14, s20
	s_addc_u32 s23, s15, 0
	s_add_u32 s24, s22, 0x1000
	s_addc_u32 s25, s23, 0
	global_load_dwordx4 v[130:133], v210, s[22:23] offset:0
	global_load_dwordx4 v[130:133], v210, s[22:23] offset:1024
	global_load_dwordx4 v[130:133], v210, s[22:23] offset:2048
	global_load_dwordx4 v[130:133], v210, s[22:23] offset:3072
	global_load_dwordx4 v[130:133], v210, s[24:25] offset:0
	global_load_dwordx4 v[130:133], v210, s[24:25] offset:1024
	global_load_dwordx4 v[130:133], v210, s[24:25] offset:2048
	global_load_dwordx4 v[130:133], v210, s[24:25] offset:3072
	v_or_b32_e32 v138, s21, v230
	global_load_dwordx4 v[134:137], v138, s[4:5] offset:0
	global_load_dwordx4 v[134:137], v138, s[4:5] offset:32
	global_load_dwordx4 v[134:137], v138, s[4:5] offset:64
	global_load_dwordx4 v[134:137], v138, s[4:5] offset:96
	global_load_dwordx4 v[134:137], v138, s[6:7] offset:0
	global_load_dwordx4 v[134:137], v138, s[6:7] offset:32
	global_load_dwordx4 v[134:137], v138, s[6:7] offset:64
	global_load_dwordx4 v[134:137], v138, s[6:7] offset:96
	s_load_dword s21, s[8:9], 0x0
	v_mfma_f32_32x32x16_bf16 v[82:97], v[78:81], v[162:165], v[82:97]
	v_exp_f32_e32 v212, v36
	v_exp_f32_e32 v213, v40
	v_exp_f32_e32 v214, v44
	v_exp_f32_e32 v215, v48
	v_mfma_f32_32x32x16_bf16 v[82:97], v[74:77], v[166:169], v[82:97]
	v_exp_f32_e32 v217, v34
	v_add_f32_e32 v251, 1.0, v212
	v_exp_f32_e32 v218, v38
	v_add_f32_e32 v252, 1.0, v213
	v_exp_f32_e32 v219, v42
	v_add_f32_e32 v253, 1.0, v214
	v_exp_f32_e32 v220, v46
	v_add_f32_e32 v254, 1.0, v215
	v_fma_f32 v240, v212, s12, v235
	v_fma_f32 v241, v213, s12, v235
	v_fma_f32 v242, v214, s12, v235
	v_fma_f32 v243, v215, s12, v235
	v_mfma_f32_32x32x16_bf16 v[82:97], v[70:73], v[170:173], v[82:97]
	v_exp_f32_e32 v221, v35
	v_fmac_f32_e32 v251, v217, v251
	v_exp_f32_e32 v222, v39
	v_fmac_f32_e32 v252, v218, v252
	v_exp_f32_e32 v223, v43
	v_fmac_f32_e32 v253, v219, v253
	v_exp_f32_e32 v224, v47
	v_fmac_f32_e32 v254, v220, v254
	v_mfma_f32_32x32x16_bf16 v[82:97], v[66:69], v[174:177], v[82:97]
	v_rcp_f32_e32 v217, v251
	v_add_f32_e32 v221, 1.0, v221
	v_rcp_f32_e32 v218, v252
	v_add_f32_e32 v222, 1.0, v222
	v_rcp_f32_e32 v219, v253
	v_add_f32_e32 v223, 1.0, v223
	v_rcp_f32_e32 v220, v254
	v_add_f32_e32 v224, 1.0, v224
	v_mfma_f32_32x32x16_bf16 v[82:97], v[62:65], v[178:181], v[82:97]
	v_rcp_f32_e32 v221, v221
	v_mul_f32_e32 v240, v240, v217
	v_rcp_f32_e32 v222, v222
	v_mul_f32_e32 v241, v241, v218
	v_rcp_f32_e32 v223, v223
	v_mul_f32_e32 v242, v242, v219
	v_rcp_f32_e32 v224, v224
	v_mul_f32_e32 v243, v243, v220
	v_mfma_f32_32x32x16_bf16 v[82:97], v[58:61], v[182:185], v[82:97]
	v_exp_f32_e32 v246, v37
	v_fma_f32 v202, v221, v202, v240
	v_exp_f32_e32 v247, v41
	v_fma_f32 v203, v222, v203, v241
	v_exp_f32_e32 v248, v45
	v_fma_f32 v204, v223, v204, v242
	v_exp_f32_e32 v249, v49
	v_fma_f32 v205, v224, v205, v243
	v_mfma_f32_32x32x16_bf16 v[82:97], v[54:57], v[186:189], v[82:97]
	v_exp_f32_e32 v212, v202
	v_add_f32_e32 v246, 1.0, v246
	v_exp_f32_e32 v213, v203
	v_add_f32_e32 v247, 1.0, v247
	v_exp_f32_e32 v214, v204
	v_add_f32_e32 v248, 1.0, v248
	v_exp_f32_e32 v215, v205
	v_add_f32_e32 v249, 1.0, v249
	v_fmac_f32_e32 v246, v246, v212
	v_fmac_f32_e32 v247, v247, v213
	v_fmac_f32_e32 v248, v248, v214
	v_fmac_f32_e32 v249, v249, v215
	v_mfma_f32_32x32x16_bf16 v[82:97], v[50:53], v[190:193], v[82:97]
	v_rcp_f32_e32 v246, v246
	v_rcp_f32_e32 v247, v247
	v_rcp_f32_e32 v248, v248
	v_rcp_f32_e32 v249, v249
	v_fma_f32 v246, -v212, v246, v246
	v_fma_f32 v247, -v213, v247, v247
	v_fma_f32 v248, -v214, v248, v248
	v_fma_f32 v249, -v215, v249, v249
	v_cvt_pk_bf16_f32 v236, v246, v247
	v_cvt_pk_bf16_f32 v237, v248, v249
	s_waitcnt lgkmcnt(0)
	v_exp_f32_e32 v212, v84
	v_exp_f32_e32 v213, v88
	v_exp_f32_e32 v214, v92
	v_exp_f32_e32 v215, v96
	v_exp_f32_e32 v217, v82
	v_add_f32_e32 v251, 1.0, v212
	v_exp_f32_e32 v218, v86
	v_add_f32_e32 v252, 1.0, v213
	v_exp_f32_e32 v219, v90
	v_add_f32_e32 v253, 1.0, v214
	v_exp_f32_e32 v220, v94
	v_add_f32_e32 v254, 1.0, v215
	v_fma_f32 v240, v212, s12, v235
	v_fma_f32 v241, v213, s12, v235
	v_fma_f32 v242, v214, s12, v235
	v_fma_f32 v243, v215, s12, v235
	v_exp_f32_e32 v221, v83
	v_fmac_f32_e32 v251, v217, v251
	v_exp_f32_e32 v222, v87
	v_fmac_f32_e32 v252, v218, v252
	v_exp_f32_e32 v223, v91
	v_fmac_f32_e32 v253, v219, v253
	v_exp_f32_e32 v224, v95
	v_fmac_f32_e32 v254, v220, v254
	v_rcp_f32_e32 v217, v251
	v_add_f32_e32 v221, 1.0, v221
	v_rcp_f32_e32 v218, v252
	v_add_f32_e32 v222, 1.0, v222
	v_rcp_f32_e32 v219, v253
	v_add_f32_e32 v223, 1.0, v223
	v_rcp_f32_e32 v220, v254
	v_add_f32_e32 v224, 1.0, v224
	v_rcp_f32_e32 v221, v221
	v_mul_f32_e32 v240, v240, v217
	v_rcp_f32_e32 v222, v222
	v_mul_f32_e32 v241, v241, v218
	v_rcp_f32_e32 v223, v223
	v_mul_f32_e32 v242, v242, v219
	v_rcp_f32_e32 v224, v224
	v_mul_f32_e32 v243, v243, v220
	v_exp_f32_e32 v246, v85
	v_fma_f32 v206, v221, v206, v240
	v_exp_f32_e32 v247, v89
	v_fma_f32 v207, v222, v207, v241
	v_exp_f32_e32 v248, v93
	v_fma_f32 v208, v223, v208, v242
	v_exp_f32_e32 v249, v97
	v_fma_f32 v209, v224, v209, v243
	v_exp_f32_e32 v212, v206
	v_add_f32_e32 v246, 1.0, v246
	v_exp_f32_e32 v213, v207
	v_add_f32_e32 v247, 1.0, v247
	v_exp_f32_e32 v214, v208
	v_add_f32_e32 v248, 1.0, v248
	v_exp_f32_e32 v215, v209
	v_add_f32_e32 v249, 1.0, v249
	v_fmac_f32_e32 v246, v246, v212
	v_fmac_f32_e32 v247, v247, v213
	v_fmac_f32_e32 v248, v248, v214
	v_fmac_f32_e32 v249, v249, v215
	v_rcp_f32_e32 v246, v246
	v_rcp_f32_e32 v247, v247
	v_rcp_f32_e32 v248, v248
	v_rcp_f32_e32 v249, v249
	v_fma_f32 v246, -v212, v246, v246
	v_fma_f32 v247, -v213, v247, v247
	v_fma_f32 v248, -v214, v248, v248
	v_fma_f32 v249, -v215, v249, v249
	v_cvt_pk_bf16_f32 v238, v246, v247
	v_cvt_pk_bf16_f32 v239, v248, v249
	ds_write_b128 v211, v[236:239] offset:8192
	s_waitcnt lgkmcnt(0)
	s_barrier
	s_waitcnt vmcnt(0)
	s_nop 7
	s_nop 7
	s_branch .Lepilogue
